# v34: v32 + ph5 state-scan loads (32 state words at the top of the phase, 32 n-vector words after the tables' first barrier) fetched behind the tables instead of at the start of the scan
# speedup vs baseline: 1.0061x; 1.0035x over previous
; #define LAS __attribute__((address_space(3)))
; __device__ __forceinline__ void ph5_tables(const Frame& F, const Args& A) {
;     unsigned char* ws = A.ws; const float* SC = (const float*)(ws + WS_SC);
;     LAS float* inclL = (LAS float*)(F.lds + T_INCL); LAS int* costL = (LAS int*)(F.lds + T_COST); LAS int* prefL = (LAS int*)(F.lds + T_PREF); LAS int* jloL = (LAS int*)(F.lds + T_JLO);
;     LAS float* thL = (LAS float*)(F.lds + T_TH); LAS float* decL = (LAS float*)(F.lds + T_DEC); LAS float* sclL = (LAS float*)(F.lds + T_SCL);
;     const int h = F.wave, l = F.lane;
;     {
;         const float v0 = SC[2048 + h * 128 + 2 * l], v1 = SC[2048 + h * 128 + 2 * l + 1]; const float sm = v0 + v1; const float incl = wave_scan_add(sm, l);
;         inclL[h * 128 + 2 * l] = incl - v1; inclL[h * 128 + 2 * l + 1] = incl;
;         const float* gq = A.in[I_FQG] + h * 128 + 2 * l; const float* gk = A.in[I_FKG] + h * 128 + 2 * l;
;         const float gqm = wave_max(fmaxf(fabsf(gq[0]), fabsf(gq[1]))), gkm = wave_max(fmaxf(fabsf(gk[0]), fabsf(gk[1])));
;         if (l == 0) thL[h] = 106.f + 2.f * 11.313708498984761f * gqm * gkm * 1.02f;
;     }
; __device__ __forceinline__ void ph5_m2(const Frame& F, const Args& A) {
;     ...
;         const int hA = ttA >> 6, rA = (ttA * 128 + 2 * l) & 8191, jA = ttA & 63, hB = ttB >> 6, rB = (ttB * 128 + 2 * l) & 8191, jB = ttB & 63;
;         const bf16* srcA = U + (size_t)hA * 128 * 8192 + rA; const bf16* srcB = U + (size_t)hB * 128 * 8192 + rB;
;         const float* snA = UN + (size_t)hA * 128 * 64 + jA; const float* snB = UN + (size_t)hB * 128 * 64 + jB;
;         f32x2_t uA[16], uB[16]; float nA[16], nB[16];
; #pragma unroll
;         for (int i = 0; i < 16; ++i) { const unsigned wa = *(const unsigned*)(srcA + (size_t)(16 * g + i) * 8192), wb = *(const unsigned*)(srcB + (size_t)(16 * g + i) * 8192);
;             uA[i] = (f32x2_t){bflo(wa), bfhi(wa)}; uB[i] = (f32x2_t){bflo(wb), bfhi(wb)};
;             nA[i] = snA[(16 * g + i) * 64]; nB[i] = snB[(16 * g + i) * 64]; }
.LBB0_529:
	v_readlane_b32 s0, v254, 9
	v_readlane_b32 s1, v254, 10
	s_cmp_lt_i32 s0, 6
	s_cselect_b64 s[0:1], -1, 0
	s_and_b64 s[80:81], s[0:1], s[2:3]
	s_andn2_b64 vcc, exec, s[80:81]
	s_cbranch_vccnz .LBB0_882
	v_mov_b32_e32 v2, v0
	s_add_u32 s0, s88, 0xb00000
	v_and_b32_e32 v14, 63, v2
	v_readlane_b32 s2, v254, 32
	v_readlane_b32 s4, v254, 16
	s_addc_u32 s1, s89, 0
	s_lshl_b32 s2, s2, 7
	v_lshlrev_b32_e32 v75, 1, v14
	s_mov_b32 s3, 0
	v_readlane_b32 s8, v254, 20
	v_readlane_b32 s9, v254, 21
	v_readlane_b32 s10, v254, 22
	v_readlane_b32 s11, v254, 23
	v_readlane_b32 s12, v254, 24
	v_readlane_b32 s13, v254, 25
	v_or_b32_e32 v4, s2, v75
	s_lshl_b64 s[2:3], s[2:3], 2
	v_readlane_b32 s14, v254, 26
	v_readlane_b32 s15, v254, 27
	s_mov_b64 s[8:9], s[12:13]
	v_readlane_b32 s5, v254, 17
	s_add_u32 s4, s8, s2
	v_add_u32_e32 v6, 0x800, v4
	s_mov_b64 s[10:11], s[14:15]
	s_addc_u32 s5, s9, s3
	v_lshlrev_b32_e32 v1, 3, v14
	global_load_dwordx2 v[16:17], v1, s[4:5]
	v_ashrrev_i32_e32 v7, 31, v6
	s_add_u32 s2, s10, s2
	s_addc_u32 s3, s11, s3
	v_lshl_add_u64 v[6:7], v[6:7], 2, s[0:1]
	global_load_dwordx2 v[18:19], v1, s[2:3]
	global_load_dwordx2 v[20:21], v[6:7], off
	v_lshlrev_b32_e32 v60, 2, v4
	v_add_u32_e32 v61, 0x1000, v60
	global_load_dwordx2 v[64:65], v60, s[0:1]
	global_load_dwordx2 v[66:67], v61, s[0:1]
	v_readlane_b32 s98, v254, 4
	s_lshl_b32 s99, s98, 7
	s_and_b32 s99, s99, 0x1f80
	v_or_b32_e32 v170, s99, v75
	s_lshr_b32 s98, s98, 6
	s_lshl_b32 s98, s98, 21
	v_lshl_add_u32 v170, v170, 1, s98
	v_readlane_b32 s99, v254, 32
	s_lshl_b32 s99, s99, 18
	v_add_u32_e32 v170, s99, v170
	v_add_u32_e32 v171, 0x800000, v170
	s_add_u32 s98, s88, 0xde00000
	s_addc_u32 s99, s89, 0
	global_load_dword v134, v170, s[98:99]
	global_load_dword v135, v171, s[98:99]
	s_add_u32 s98, s98, 0x4000
	s_addc_u32 s99, s99, 0
	global_load_dword v136, v170, s[98:99]
	global_load_dword v137, v171, s[98:99]
	s_add_u32 s98, s98, 0x4000
	s_addc_u32 s99, s99, 0
	global_load_dword v138, v170, s[98:99]
	global_load_dword v139, v171, s[98:99]
	s_add_u32 s98, s98, 0x4000
	s_addc_u32 s99, s99, 0
	global_load_dword v140, v170, s[98:99]
	global_load_dword v141, v171, s[98:99]
	s_add_u32 s98, s98, 0x4000
	s_addc_u32 s99, s99, 0
	global_load_dword v142, v170, s[98:99]
	global_load_dword v143, v171, s[98:99]
	s_add_u32 s98, s98, 0x4000
	s_addc_u32 s99, s99, 0
	global_load_dword v144, v170, s[98:99]
	global_load_dword v145, v171, s[98:99]
	s_add_u32 s98, s98, 0x4000
	s_addc_u32 s99, s99, 0
	global_load_dword v146, v170, s[98:99]
	global_load_dword v147, v171, s[98:99]
	s_add_u32 s98, s98, 0x4000
	s_addc_u32 s99, s99, 0
	global_load_dword v148, v170, s[98:99]
	global_load_dword v149, v171, s[98:99]
	s_add_u32 s98, s98, 0x4000
	s_addc_u32 s99, s99, 0
	global_load_dword v150, v170, s[98:99]
	global_load_dword v151, v171, s[98:99]
	s_add_u32 s98, s98, 0x4000
	s_addc_u32 s99, s99, 0
	global_load_dword v152, v170, s[98:99]
	global_load_dword v153, v171, s[98:99]
	s_add_u32 s98, s98, 0x4000
	s_addc_u32 s99, s99, 0
	global_load_dword v154, v170, s[98:99]
	global_load_dword v155, v171, s[98:99]
	s_add_u32 s98, s98, 0x4000
	s_addc_u32 s99, s99, 0
	global_load_dword v156, v170, s[98:99]
	global_load_dword v157, v171, s[98:99]
	s_add_u32 s98, s98, 0x4000
	s_addc_u32 s99, s99, 0
	global_load_dword v158, v170, s[98:99]
	global_load_dword v159, v171, s[98:99]
	s_add_u32 s98, s98, 0x4000
	s_addc_u32 s99, s99, 0
	global_load_dword v160, v170, s[98:99]
	global_load_dword v161, v171, s[98:99]
	s_add_u32 s98, s98, 0x4000
	s_addc_u32 s99, s99, 0
	global_load_dword v162, v170, s[98:99]
	global_load_dword v163, v171, s[98:99]
	s_add_u32 s98, s98, 0x4000
	s_addc_u32 s99, s99, 0
	global_load_dword v164, v170, s[98:99]
	global_load_dword v165, v171, s[98:99]
	v_mbcnt_lo_u32_b32 v1, -1, 0
	v_mbcnt_hi_u32_b32 v1, -1, v1
	v_and_b32_e32 v3, 64, v1
	v_add_u32_e32 v5, -1, v1
	v_add_u32_e32 v6, -2, v1
	v_cmp_lt_i32_e32 vcc, v5, v3
	v_add_u32_e32 v7, -4, v1
	v_add_u32_e32 v8, -8, v1
	v_cndmask_b32_e32 v5, v5, v1, vcc
	v_cmp_lt_i32_e32 vcc, v6, v3
	v_add_u32_e32 v9, -16, v1
	v_subrev_u32_e32 v10, 32, v1
	v_cndmask_b32_e32 v6, v6, v1, vcc
	v_cmp_lt_i32_e32 vcc, v7, v3
	v_xor_b32_e32 v13, 1, v1
	v_add_u32_e32 v28, 64, v3
	v_cndmask_b32_e32 v7, v7, v1, vcc
	v_cmp_lt_i32_e32 vcc, v8, v3
	v_xor_b32_e32 v15, 2, v1
	v_xor_b32_e32 v22, 4, v1
	v_cndmask_b32_e32 v8, v8, v1, vcc
	v_cmp_lt_i32_e32 vcc, v9, v3
	v_lshlrev_b32_e32 v12, 2, v5
	v_xor_b32_e32 v23, 8, v1
	v_cndmask_b32_e32 v26, v9, v1, vcc
	v_cmp_lt_i32_e32 vcc, v10, v3
	v_lshlrev_b32_e32 v11, 2, v6
	v_xor_b32_e32 v24, 16, v1
	v_cndmask_b32_e32 v27, v10, v1, vcc
	v_cmp_lt_i32_e32 vcc, v13, v28
	v_lshlrev_b32_e32 v10, 2, v7
	v_xor_b32_e32 v25, 32, v1
	v_cndmask_b32_e32 v5, v1, v13, vcc
	v_cmp_lt_i32_e32 vcc, v15, v28
	v_cmp_eq_u32_e64 s[2:3], 0, v14
	v_readlane_b32 s6, v254, 18
	v_cndmask_b32_e32 v6, v1, v15, vcc
	v_cmp_lt_i32_e32 vcc, v22, v28
	v_readlane_b32 s7, v254, 19
	v_cmp_gt_u32_e64 s[6:7], 2, v14
	v_cndmask_b32_e32 v7, v1, v22, vcc
	v_cmp_lt_i32_e32 vcc, v23, v28
	v_cmp_gt_u32_e64 s[8:9], 4, v14
	v_lshlrev_b32_e32 v9, 2, v8
	v_cndmask_b32_e32 v13, v1, v23, vcc
	v_cmp_lt_i32_e32 vcc, v24, v28
	v_cmp_gt_u32_e64 s[10:11], 8, v14
	v_lshlrev_b32_e32 v8, 2, v26
	v_cndmask_b32_e32 v15, v1, v24, vcc
	v_cmp_lt_i32_e32 vcc, v25, v28
	v_cmp_gt_u32_e64 s[12:13], 16, v14
	v_lshlrev_b32_e32 v3, 2, v27
	v_cndmask_b32_e32 v22, v1, v25, vcc
	v_lshlrev_b32_e32 v1, 2, v5
	v_lshlrev_b32_e32 v5, 2, v6
	v_lshlrev_b32_e32 v6, 2, v7
	v_lshlrev_b32_e32 v7, 2, v13
	v_lshlrev_b32_e32 v13, 2, v15
	v_cmp_gt_u32_e64 s[14:15], 32, v14
	v_readlane_b32 s16, v254, 28
	v_readlane_b32 s17, v254, 29
	v_readlane_b32 s18, v254, 30
	v_readlane_b32 s19, v254, 31
	s_waitcnt vmcnt(32)
; __device__ __forceinline__ void ph5_tables(const Frame& F, const Args& A) {
;     ...
;         const float v0 = SC[2048 + h * 128 + 2 * l], v1 = SC[2048 + h * 128 + 2 * l + 1]; const float sm = v0 + v1; const float incl = wave_scan_add(sm, l);
;         inclL[h * 128 + 2 * l] = incl - v1; inclL[h * 128 + 2 * l + 1] = incl;
;         const float* gq = A.in[I_FQG] + h * 128 + 2 * l; const float* gk = A.in[I_FKG] + h * 128 + 2 * l;
;         const float gqm = wave_max(fmaxf(fabsf(gq[0]), fabsf(gq[1]))), gkm = wave_max(fmaxf(fabsf(gk[0]), fabsf(gk[1])));
;         if (l == 0) thL[h] = 106.f + 2.f * 11.313708498984761f * gqm * gkm * 1.02f;
;     }
;     {
;         const float g0 = SC[h * 128 + 2 * l], g1 = SC[h * 128 + 2 * l + 1], a0 = SC[1024 + h * 128 + 2 * l], a1 = SC[1024 + h * 128 + 2 * l + 1];
;         const float gi1 = wave_scan_add(g0 + g1, l), gi0 = gi1 - g1, gx0 = gi0 - g0;
;         const float val0 = a0 - gi0, val1 = a1 - gi1;
;         const float pmi = wave_scan_max(fmaxf(val0, val1), l); float pme = __shfl_up(pmi, 1); if (l == 0) pme = -INFINITY;
;         const float M0 = fmaxf(0.f, pme), M1 = fmaxf(M0, val0), M2 = fmaxf(M1, val1);
;         const float m0 = M0 + gx0, m1 = M1 + gi0, m2 = M2 + gi1;
	v_max_f32_e64 v15, |v17|, |v17|
	v_max_f32_e64 v16, |v16|, |v16|
	v_max_f32_e32 v15, v16, v15
	ds_bpermute_b32 v16, v1, v15
	v_max_f32_e64 v17, |v19|, |v19|
	v_add_f32_e32 v19, v20, v21
	ds_bpermute_b32 v20, v12, v19
	v_max_f32_e64 v18, |v18|, |v18|
	v_max_f32_e32 v17, v18, v17
	s_waitcnt lgkmcnt(1)
	v_max_f32_e32 v16, v16, v16
	ds_bpermute_b32 v18, v1, v17
	v_max_f32_e32 v15, v15, v16
	s_waitcnt lgkmcnt(1)
	v_add_f32_e32 v16, v19, v20
	ds_bpermute_b32 v20, v5, v15
	v_cndmask_b32_e64 v16, v16, v19, s[2:3]
	ds_bpermute_b32 v19, v11, v16
	s_waitcnt lgkmcnt(2)
	v_max_f32_e32 v18, v18, v18
	v_max_f32_e32 v17, v17, v18
	s_waitcnt lgkmcnt(1)
	v_max_f32_e32 v18, v20, v20
	ds_bpermute_b32 v5, v5, v17
	v_max_f32_e32 v15, v15, v18
	s_waitcnt lgkmcnt(1)
	v_add_f32_e32 v18, v16, v19
	ds_bpermute_b32 v19, v6, v15
	v_cndmask_b32_e64 v16, v18, v16, s[6:7]
	ds_bpermute_b32 v18, v10, v16
	s_waitcnt lgkmcnt(2)
	v_max_f32_e32 v5, v5, v5
	v_max_f32_e32 v5, v17, v5
	s_waitcnt lgkmcnt(1)
	v_max_f32_e32 v17, v19, v19
	ds_bpermute_b32 v6, v6, v5
	v_max_f32_e32 v15, v15, v17
	s_waitcnt lgkmcnt(1)
	v_add_f32_e32 v17, v16, v18
	v_cndmask_b32_e64 v16, v17, v16, s[8:9]
	ds_bpermute_b32 v17, v9, v16
	s_waitcnt lgkmcnt(1)
	v_max_f32_e32 v6, v6, v6
	v_max_f32_e32 v5, v5, v6
	ds_bpermute_b32 v18, v7, v15
	ds_bpermute_b32 v6, v7, v5
	s_waitcnt lgkmcnt(2)
	v_add_f32_e32 v7, v16, v17
	v_cndmask_b32_e64 v7, v7, v16, s[10:11]
	ds_bpermute_b32 v16, v8, v7
	s_waitcnt lgkmcnt(2)
	v_max_f32_e32 v17, v18, v18
	v_max_f32_e32 v15, v15, v17
	ds_bpermute_b32 v17, v13, v15
	s_waitcnt lgkmcnt(2)
	v_max_f32_e32 v6, v6, v6
	s_waitcnt lgkmcnt(1)
	v_add_f32_e32 v16, v7, v16
	v_cndmask_b32_e64 v7, v16, v7, s[12:13]
	ds_bpermute_b32 v16, v3, v7
	v_max_f32_e32 v6, v5, v6
	ds_bpermute_b32 v13, v13, v6
	s_waitcnt lgkmcnt(2)
	v_max_f32_e32 v5, v17, v17
	v_max_f32_e32 v5, v15, v5
	s_waitcnt lgkmcnt(1)
	v_add_f32_e32 v15, v7, v16
	v_cndmask_b32_e64 v17, v15, v7, s[14:15]
	s_waitcnt lgkmcnt(0)
	v_max_f32_e32 v7, v13, v13
	v_lshlrev_b32_e32 v16, 2, v22
	v_max_f32_e32 v7, v6, v7
	ds_bpermute_b32 v15, v16, v5
	ds_bpermute_b32 v13, v16, v7
	v_lshl_add_u32 v6, v4, 2, 0
	v_sub_f32_e32 v16, v17, v21
	v_add_u32_e32 v18, 0x19400, v6
	ds_write_b64 v18, v[16:17]
	s_and_saveexec_b64 s[4:5], s[2:3]
	s_cbranch_execz .LBB0_532
	v_readlane_b32 s16, v254, 32
	s_waitcnt lgkmcnt(2)
	v_max_f32_e32 v15, v15, v15
	v_max_f32_e32 v5, v5, v5
	s_lshl_b32 s16, s16, 2
	v_max_f32_e32 v5, v5, v15
	s_waitcnt lgkmcnt(1)
	v_max_f32_e32 v13, v13, v13
	v_max_f32_e32 v7, v7, v7
	s_add_i32 s16, s16, 0
	v_mul_f32_e32 v5, 0x41b504f3, v5
	v_max_f32_e32 v7, v7, v13
	s_add_i32 s16, s16, 0x1b020
	v_mul_f32_e32 v5, v5, v7
	v_mov_b32_e32 v7, 0x42d40000
	v_fmac_f32_e32 v7, 0x3f828f5c, v5
	v_mov_b32_e32 v5, s16
	ds_write_b32 v5, v7
.LBB0_532:
	s_or_b64 exec, exec, s[4:5]
	v_mov_b32_e32 v5, 0
	v_lshl_add_u64 v[16:17], v[4:5], 2, s[0:1]
	v_mov_b64_e32 v[16:17], v[64:65]
	v_add_u32_e32 v18, 0x400, v4
	v_ashrrev_i32_e32 v19, 31, v18
	v_lshl_add_u64 v[18:19], v[18:19], 2, s[0:1]
	v_mov_b64_e32 v[18:19], v[66:67]
	v_add_u32_e32 v24, 0x1b400, v6
	v_add_u32_e32 v25, 0x1c400, v6
	s_mov_b32 s0, 0x3fb8aa3b
	s_mov_b32 s1, 0xc2ce8ed0
	s_mov_b32 s4, 0x42b17218
	v_mov_b32_e32 v23, 0x7f800000
	v_readlane_b32 s5, v254, 4
	s_cmp_eq_u32 s5, 0
	s_cselect_b64 s[18:19], -1, 0
	s_cmp_lg_u32 s5, 0
	s_waitcnt vmcnt(33)
	v_add_f32_e32 v7, v16, v17
	s_waitcnt lgkmcnt(1)
	ds_bpermute_b32 v13, v12, v7
	s_waitcnt lgkmcnt(0)
	v_add_f32_e32 v13, v7, v13
	v_cndmask_b32_e64 v7, v13, v7, s[2:3]
	ds_bpermute_b32 v13, v11, v7
	s_waitcnt lgkmcnt(0)
	v_add_f32_e32 v13, v7, v13
	v_cndmask_b32_e64 v7, v13, v7, s[6:7]
	ds_bpermute_b32 v13, v10, v7
	s_waitcnt lgkmcnt(0)
	v_add_f32_e32 v13, v7, v13
	v_cndmask_b32_e64 v7, v13, v7, s[8:9]
	ds_bpermute_b32 v13, v9, v7
	s_waitcnt lgkmcnt(0)
	v_add_f32_e32 v13, v7, v13
	v_cndmask_b32_e64 v7, v13, v7, s[10:11]
	ds_bpermute_b32 v13, v8, v7
	s_waitcnt lgkmcnt(0)
	v_add_f32_e32 v13, v7, v13
	v_cndmask_b32_e64 v7, v13, v7, s[12:13]
	ds_bpermute_b32 v13, v3, v7
	s_waitcnt lgkmcnt(0)
	v_add_f32_e32 v13, v7, v13
	v_cndmask_b32_e64 v13, v13, v7, s[14:15]
	v_sub_f32_e32 v7, v13, v17
	s_waitcnt vmcnt(32)
	v_sub_f32_e32 v15, v19, v13
	v_sub_f32_e32 v21, v18, v7
	v_max_f32_e32 v20, v21, v15
	ds_bpermute_b32 v22, v12, v20
	s_waitcnt lgkmcnt(0)
	v_max_f32_e32 v22, v22, v22
	v_max_f32_e32 v22, v20, v22
	v_cndmask_b32_e64 v20, v22, v20, s[2:3]
	ds_bpermute_b32 v22, v11, v20
	s_waitcnt lgkmcnt(0)
	v_max_f32_e32 v22, v22, v22
	v_max_f32_e32 v22, v20, v22
	v_cndmask_b32_e64 v20, v22, v20, s[6:7]
	ds_bpermute_b32 v22, v10, v20
	s_waitcnt lgkmcnt(0)
	v_max_f32_e32 v22, v22, v22
	v_max_f32_e32 v22, v20, v22
	v_cndmask_b32_e64 v20, v22, v20, s[8:9]
	ds_bpermute_b32 v22, v9, v20
	s_waitcnt lgkmcnt(0)
	v_max_f32_e32 v22, v22, v22
	v_max_f32_e32 v22, v20, v22
	v_cndmask_b32_e64 v20, v22, v20, s[10:11]
	ds_bpermute_b32 v22, v8, v20
	s_waitcnt lgkmcnt(0)
	v_max_f32_e32 v22, v22, v22
	v_max_f32_e32 v22, v20, v22
	v_cndmask_b32_e64 v20, v22, v20, s[12:13]
	ds_bpermute_b32 v22, v3, v20
	v_max_f32_e32 v6, v20, v20
	s_waitcnt lgkmcnt(0)
	v_max_f32_e32 v22, v22, v22
	v_max_f32_e32 v6, v6, v22
	v_cndmask_b32_e64 v6, v6, v20, s[14:15]
	ds_bpermute_b32 v20, v12, v6
	v_sub_f32_e32 v6, v7, v16
	s_waitcnt lgkmcnt(0)
; __device__ __forceinline__ void ph5_tables(const Frame& F, const Args& A) {
;     ...
;         decL[h * 128 + 2 * l] = expf(g0 + m0 - m1); sclL[h * 128 + 2 * l] = expf(a0 - m1);
;         decL[h * 128 + 2 * l + 1] = expf(g1 + m1 - m2); sclL[h * 128 + 2 * l + 1] = expf(a1 - m2);
;         if (F.vcu == 0) { float* MST = (float*)(ws + WS_SC) + 3072; MST[h * 128 + 2 * l] = m0; MST[h * 128 + 2 * l + 1] = m1; }
;     }
;     __syncthreads();
;     int mycost = 0;
;     if (F.tid < 256) { const int i = F.tid, hh = i >> 5, qb = i & 31; const float fref = qb ? inclL[hh * 128 + 4 * qb - 1] : 0.f, th = thL[hh];
;         int lo = 0, hi2 = 4 * qb;
;         while (lo < hi2) { const int mid = (lo + hi2) >> 1; if (fref - inclL[hh * 128 + mid] < -th) lo = mid + 1; else hi2 = mid; }
;         jloL[i] = lo; mycost = 4 * (qb + 1) - lo; costL[i] = mycost; }
; __device__ __forceinline__ void ph5_m2(const Frame& F, const Args& A) {
;     ...
;         for (int i = 0; i < 16; ++i) { const unsigned wa = *(const unsigned*)(srcA + (size_t)(16 * g + i) * 8192), wb = *(const unsigned*)(srcB + (size_t)(16 * g + i) * 8192);
;             uA[i] = (f32x2_t){bflo(wa), bfhi(wa)}; uB[i] = (f32x2_t){bflo(wb), bfhi(wb)};
;             nA[i] = snA[(16 * g + i) * 64]; nB[i] = snB[(16 * g + i) * 64]; }
	v_max_f32_e32 v20, v20, v20
	v_max_f32_e32 v20, 0, v20
	v_cndmask_b32_e64 v20, v20, 0, s[2:3]
	v_max_f32_e32 v21, v20, v21
	v_max_f32_e32 v15, v21, v15
	v_pk_add_f32 v[6:7], v[20:21], v[6:7]
	v_add_f32_e32 v13, v13, v15
	v_pk_add_f32 v[16:17], v[16:17], v[6:7]
	v_sub_f32_e32 v15, v18, v7
	v_sub_f32_e32 v18, v16, v7
	v_mul_f32_e32 v16, 0x3fb8aa3b, v15
	v_sub_f32_e32 v17, v17, v13
	v_sub_f32_e32 v13, v19, v13
	v_mul_f32_e32 v19, 0x3fb8aa3b, v18
	v_fma_f32 v20, v15, s0, -v16
	v_rndne_f32_e32 v21, v16
	v_fma_f32 v27, v18, s0, -v19
	v_rndne_f32_e32 v28, v19
	v_fmac_f32_e32 v20, 0x32a5705f, v15
	v_sub_f32_e32 v16, v16, v21
	v_mul_f32_e32 v22, 0x3fb8aa3b, v17
	v_fmac_f32_e32 v27, 0x32a5705f, v18
	v_sub_f32_e32 v19, v19, v28
	v_add_f32_e32 v16, v16, v20
	v_mul_f32_e32 v26, 0x3fb8aa3b, v13
	v_cvt_i32_f32_e32 v21, v21
	v_fma_f32 v29, v17, s0, -v22
	v_rndne_f32_e32 v30, v22
	v_add_f32_e32 v19, v19, v27
	v_exp_f32_e32 v16, v16
	v_fma_f32 v31, v13, s0, -v26
	v_rndne_f32_e32 v32, v26
	v_cvt_i32_f32_e32 v28, v28
	v_fmac_f32_e32 v29, 0x32a5705f, v17
	v_sub_f32_e32 v20, v22, v30
	v_exp_f32_e32 v19, v19
	v_fmac_f32_e32 v31, 0x32a5705f, v13
	v_sub_f32_e32 v26, v26, v32
	v_add_f32_e32 v20, v20, v29
	v_cvt_i32_f32_e32 v22, v30
	v_add_f32_e32 v26, v26, v31
	v_exp_f32_e32 v20, v20
	v_cvt_i32_f32_e32 v30, v32
	v_exp_f32_e32 v26, v26
	v_ldexp_f32 v16, v16, v21
	v_cmp_ngt_f32_e32 vcc, s1, v15
	v_ldexp_f32 v19, v19, v28
	v_ldexp_f32 v20, v20, v22
	v_cndmask_b32_e32 v16, 0, v16, vcc
	v_cmp_ngt_f32_e32 vcc, s1, v18
	v_ldexp_f32 v21, v26, v30
	s_nop 0
	v_cndmask_b32_e32 v19, 0, v19, vcc
	v_cmp_nlt_f32_e32 vcc, s4, v15
	s_nop 1
	v_cndmask_b32_e32 v16, v23, v16, vcc
	v_cmp_ngt_f32_e32 vcc, s1, v17
	s_nop 1
	v_cndmask_b32_e32 v15, 0, v20, vcc
	v_cmp_ngt_f32_e32 vcc, s1, v13
	s_nop 1
	v_cndmask_b32_e32 v20, 0, v21, vcc
	v_cmp_nlt_f32_e32 vcc, s4, v18
	s_nop 1
	v_cndmask_b32_e32 v18, v23, v19, vcc
	v_cmp_nlt_f32_e32 vcc, s4, v17
	s_nop 1
	v_cndmask_b32_e32 v19, v23, v15, vcc
	v_cmp_nlt_f32_e32 vcc, s4, v13
	s_nop 1
	v_cndmask_b32_e32 v17, v23, v20, vcc
	ds_write_b64 v24, v[18:19]
	ds_write_b64 v25, v[16:17]
	s_cbranch_scc1 .LBB0_534
	v_lshl_add_u64 v[16:17], v[4:5], 2, s[88:89]
	v_add_co_u32_e32 v16, vcc, 0xb03000, v16
	s_nop 1
	v_addc_co_u32_e32 v17, vcc, 0, v17, vcc
	global_store_dwordx2 v[16:17], v[6:7], off
.LBB0_534:
	s_movk_i32 s0, 0x100
	v_cmp_gt_i32_e64 s[4:5], s0, v2
	s_waitcnt lgkmcnt(0)
	s_barrier
	v_readlane_b32 s98, v254, 4
	s_lshr_b32 s99, s98, 6
	s_lshl_b32 s99, s99, 15
	s_and_b32 s98, s98, 63
	s_lshl_b32 s98, s98, 2
	s_add_i32 s98, s98, s99
	v_readlane_b32 s99, v254, 32
	s_lshl_b32 s99, s99, 12
	s_add_i32 s98, s98, s99
	s_add_i32 s98, s98, 0xf00000
	s_add_u32 s98, s88, s98
	s_addc_u32 s99, s89, 0
	v_mov_b32_e32 v168, 0
	v_mov_b32_e32 v169, 0x20000
	global_load_dword v172, v168, s[98:99]
	global_load_dword v173, v169, s[98:99]
	global_load_dword v174, v168, s[98:99] offset:256
	global_load_dword v175, v169, s[98:99] offset:256
	global_load_dword v176, v168, s[98:99] offset:512
	global_load_dword v177, v169, s[98:99] offset:512
	global_load_dword v178, v168, s[98:99] offset:768
	global_load_dword v179, v169, s[98:99] offset:768
	global_load_dword v180, v168, s[98:99] offset:1024
	global_load_dword v181, v169, s[98:99] offset:1024
	global_load_dword v182, v168, s[98:99] offset:1280
	global_load_dword v183, v169, s[98:99] offset:1280
	global_load_dword v184, v168, s[98:99] offset:1536
	global_load_dword v185, v169, s[98:99] offset:1536
	global_load_dword v186, v168, s[98:99] offset:1792
	global_load_dword v187, v169, s[98:99] offset:1792
	global_load_dword v188, v168, s[98:99] offset:2048
	global_load_dword v189, v169, s[98:99] offset:2048
	global_load_dword v190, v168, s[98:99] offset:2304
	global_load_dword v191, v169, s[98:99] offset:2304
	global_load_dword v192, v168, s[98:99] offset:2560
	global_load_dword v193, v169, s[98:99] offset:2560
	global_load_dword v194, v168, s[98:99] offset:2816
	global_load_dword v195, v169, s[98:99] offset:2816
	global_load_dword v196, v168, s[98:99] offset:3072
	global_load_dword v197, v169, s[98:99] offset:3072
	global_load_dword v198, v168, s[98:99] offset:3328
	global_load_dword v199, v169, s[98:99] offset:3328
	global_load_dword v200, v168, s[98:99] offset:3584
	global_load_dword v201, v169, s[98:99] offset:3584
	global_load_dword v202, v168, s[98:99] offset:3840
	global_load_dword v203, v169, s[98:99] offset:3840
	s_and_saveexec_b64 s[0:1], s[4:5]
	s_cbranch_execz .LBB0_542
	v_and_b32_e32 v5, 31, v2
	v_ashrrev_i32_e32 v7, 5, v2
	v_cmp_ne_u32_e32 vcc, 0, v5
	v_mov_b32_e32 v4, 0
	v_mov_b32_e32 v6, 0
	s_and_saveexec_b64 s[20:21], vcc
	s_add_i32 s16, 0, 0x19400
	v_lshl_add_u32 v6, v7, 9, s16
	v_lshlrev_b32_e32 v13, 4, v5
	v_add3_u32 v6, v6, v13, -4
	ds_read_b32 v6, v6
	s_or_b64 exec, exec, s[20:21]
	v_lshlrev_b32_e32 v5, 2, v5
	s_and_saveexec_b64 s[20:21], vcc
	s_cbranch_execz .LBB0_541
	v_lshl_add_u32 v4, v7, 2, 0
	v_add_u32_e32 v4, 0x1b020, v4
	ds_read_b32 v13, v4
	s_add_i32 s16, 0, 0x19400
	v_lshl_add_u32 v7, v7, 9, s16
	v_mov_b32_e32 v4, 0
	s_mov_b64 s[22:23], 0
	v_mov_b32_e32 v15, v5

; __device__ __forceinline__ void ph5_m2(const Frame& F, const Args& A) {
;     ...
;     for (int task0 = F.vcu; task0 < NT_C; task0 += 2 * F.G) {
;         const bool hasB = task0 + F.G < NT_C;
;         const int ttA = task0, ttB = hasB ? task0 + F.G : task0;
;         const int hA = ttA >> 6, rA = (ttA * 128 + 2 * l) & 8191, jA = ttA & 63, hB = ttB >> 6, rB = (ttB * 128 + 2 * l) & 8191, jB = ttB & 63;
;         const bf16* srcA = U + (size_t)hA * 128 * 8192 + rA; const bf16* srcB = U + (size_t)hB * 128 * 8192 + rB;
;         const float* snA = UN + (size_t)hA * 128 * 64 + jA; const float* snB = UN + (size_t)hB * 128 * 64 + jB;
;         f32x2_t uA[16], uB[16]; float nA[16], nB[16];
; #pragma unroll
;         for (int i = 0; i < 16; ++i) { const unsigned wa = *(const unsigned*)(srcA + (size_t)(16 * g + i) * 8192), wb = *(const unsigned*)(srcB + (size_t)(16 * g + i) * 8192);
;             uA[i] = (f32x2_t){bflo(wa), bfhi(wa)}; uB[i] = (f32x2_t){bflo(wb), bfhi(wb)};
;             nA[i] = snA[(16 * g + i) * 64]; nB[i] = snB[(16 * g + i) * 64]; }
;         float ApA = 1.f, ApB = 1.f, BnA = 0.f, BnB = 0.f; f32x2_t BpA = {0.f, 0.f}, BpB = {0.f, 0.f};
; #pragma unroll
;         for (int i = 0; i < 16; ++i) { const float dA = decL[hA * 128 + 16 * g + i], sA = sclL[hA * 128 + 16 * g + i], dB = decL[hB * 128 + 16 * g + i], sB = sclL[hB * 128 + 16 * g + i];
;             ApA *= dA; BpA = BpA * dA + uA[i] * sA; BnA = BnA * dA + nA[i] * sA; ApB *= dB; BpB = BpB * dB + uB[i] * sB; BnB = BnB * dB + nB[i] * sB; }
.LBB0_583:
	v_readlane_b32 s4, v254, 49
	s_add_i32 s6, s89, s4
	s_cmpk_lt_i32 s6, 0x200
	s_cselect_b64 s[50:51], -1, 0
	s_and_b64 s[4:5], s[50:51], exec
	s_cselect_b32 s5, s6, s89
	s_ashr_i32 s4, s89, 6
	s_lshl_b32 s6, s89, 7
	s_lshl_b32 s8, s5, 7
	s_and_b32 s6, s6, 0x1f80
	s_ashr_i32 s92, s5, 6
	s_and_b32 s8, s8, 0x1f80
	s_and_b32 s11, s5, 63
	s_ashr_i32 s5, s4, 31
	v_or_b32_e32 v2, s6, v75
	s_and_b32 s6, s89, 63
	v_or_b32_e32 v4, s8, v75
	s_lshl_b64 s[8:9], s[4:5], 21
	v_readlane_b32 s10, v255, 7
	s_add_u32 s8, s10, s8
	v_readlane_b32 s12, v255, 9
	s_addc_u32 s9, s12, s9
	v_lshlrev_b32_e32 v2, 1, v2
	s_ashr_i32 s93, s92, 31
	v_lshl_add_u64 v[66:67], s[8:9], 0, v[2:3]
	s_lshl_b64 s[8:9], s[92:93], 21
	s_add_u32 s8, s10, s8
	s_addc_u32 s9, s12, s9
	v_lshlrev_b32_e32 v62, 1, v4
	v_mov_b32_e32 v63, v3
	v_lshl_add_u64 v[68:69], s[8:9], 0, v[62:63]
	s_lshl_b64 s[8:9], s[4:5], 15
	v_readlane_b32 s14, v255, 11
	s_add_u32 s8, s14, s8
	v_readlane_b32 s15, v255, 13
	s_addc_u32 s10, s15, s9
	s_lshl_b32 s44, s6, 2
	s_add_u32 s9, s8, s44
	s_addc_u32 s10, s10, 0
	s_lshl_b64 s[12:13], s[92:93], 15
	s_add_u32 s6, s14, s12
	s_addc_u32 s8, s15, s13
	s_lshl_b32 s56, s11, 2
	v_readlane_b32 s12, v254, 52
	s_add_u32 s6, s6, s56
	v_readlane_b32 s13, v254, 53
	s_addc_u32 s8, s8, 0
	s_lshl_b64 s[12:13], s[12:13], 1
	s_waitcnt vmcnt(0)
	v_lshl_add_u64 v[4:5], v[66:67], 0, s[12:13]
	v_mov_b32_e32 v6, v134
	v_lshl_add_u64 v[4:5], v[68:69], 0, s[12:13]
	v_mov_b32_e32 v4, v135
	s_add_u32 s12, s9, s48
	s_addc_u32 s13, s10, s49
	v_mov_b32_e32 v82, v172
	s_add_u32 s12, s6, s48
	s_addc_u32 s13, s8, s49
	v_mov_b32_e32 v113, v173
	v_readlane_b32 s12, v254, 54
	v_readlane_b32 s13, v254, 55
	s_lshl_b64 s[12:13], s[12:13], 1
	s_mov_b64 s[24:25], s[18:19]
	s_mov_b64 s[22:23], s[20:21]
	v_readlane_b32 s16, v255, 15
	v_readlane_b32 s17, v255, 16
	v_lshlrev_b32_e32 v64, 16, v6
	v_and_b32_e32 v65, 0xffff0000, v6
	v_lshlrev_b32_e32 v58, 16, v4
	v_and_b32_e32 v59, 0xffff0000, v4
	v_lshl_add_u64 v[4:5], v[66:67], 0, s[12:13]
	v_mov_b32_e32 v6, v136
	v_lshl_add_u64 v[4:5], v[68:69], 0, s[12:13]
	v_mov_b32_e32 v4, v137
	s_add_u32 s12, s9, s52
	s_addc_u32 s13, s10, s53
	v_mov_b32_e32 v114, v174
	s_add_u32 s12, s6, s52
	s_addc_u32 s13, s8, s53
	v_mov_b32_e32 v111, v175
	v_readlane_b32 s12, v254, 56
	v_readlane_b32 s13, v254, 57
	s_lshl_b64 s[12:13], s[12:13], 1
	v_lshlrev_b32_e32 v60, 16, v6
	v_and_b32_e32 v61, 0xffff0000, v6
	v_lshlrev_b32_e32 v54, 16, v4
	v_and_b32_e32 v55, 0xffff0000, v4
	v_lshl_add_u64 v[4:5], v[66:67], 0, s[12:13]
	v_mov_b32_e32 v6, v138
	v_lshl_add_u64 v[4:5], v[68:69], 0, s[12:13]
	v_mov_b32_e32 v4, v139
	s_add_u32 s12, s9, s54
	s_addc_u32 s13, s10, s55
	v_mov_b32_e32 v112, v176
	s_add_u32 s12, s6, s54
	s_addc_u32 s13, s8, s55
	v_mov_b32_e32 v109, v177
	s_lshl_b64 s[12:13], s[20:21], 1
	v_lshlrev_b32_e32 v56, 16, v6
	v_and_b32_e32 v57, 0xffff0000, v6
	v_lshlrev_b32_e32 v50, 16, v4
	v_and_b32_e32 v51, 0xffff0000, v4
	v_lshl_add_u64 v[4:5], v[66:67], 0, s[12:13]
	v_mov_b32_e32 v6, v140
	v_lshl_add_u64 v[4:5], v[68:69], 0, s[12:13]
	v_mov_b32_e32 v4, v141
	s_add_u32 s12, s9, s58
	s_addc_u32 s13, s10, s59
	v_mov_b32_e32 v110, v178
	s_add_u32 s12, s6, s58
	s_addc_u32 s13, s8, s59
	v_mov_b32_e32 v107, v179
	s_lshl_b64 s[12:13], s[18:19], 1
	v_lshlrev_b32_e32 v52, 16, v6
	v_and_b32_e32 v53, 0xffff0000, v6
	v_lshlrev_b32_e32 v46, 16, v4
	v_and_b32_e32 v47, 0xffff0000, v4
	v_lshl_add_u64 v[4:5], v[66:67], 0, s[12:13]
	v_mov_b32_e32 v6, v142
	v_lshl_add_u64 v[4:5], v[68:69], 0, s[12:13]
	v_mov_b32_e32 v4, v143
	s_add_u32 s12, s9, s60
	s_addc_u32 s13, s10, s61
	v_mov_b32_e32 v108, v180
	s_add_u32 s12, s6, s60
	s_addc_u32 s13, s8, s61
	v_mov_b32_e32 v105, v181
	v_readlane_b32 s12, v254, 58
	v_readlane_b32 s13, v254, 59
	s_lshl_b64 s[12:13], s[12:13], 1
	v_lshlrev_b32_e32 v48, 16, v6
	v_and_b32_e32 v49, 0xffff0000, v6
	v_lshlrev_b32_e32 v42, 16, v4
	v_and_b32_e32 v43, 0xffff0000, v4
	v_lshl_add_u64 v[4:5], v[66:67], 0, s[12:13]
	v_mov_b32_e32 v6, v144
	v_lshl_add_u64 v[4:5], v[68:69], 0, s[12:13]
	v_mov_b32_e32 v4, v145
	s_add_u32 s12, s9, s62
	s_addc_u32 s13, s10, s63
	v_mov_b32_e32 v106, v182
	s_add_u32 s12, s6, s62
	s_addc_u32 s13, s8, s63
	v_mov_b32_e32 v103, v183
	v_readlane_b32 s12, v254, 60
	v_readlane_b32 s13, v254, 61
	s_lshl_b64 s[12:13], s[12:13], 1
	v_lshlrev_b32_e32 v44, 16, v6
	v_and_b32_e32 v45, 0xffff0000, v6
	v_lshlrev_b32_e32 v38, 16, v4
	v_and_b32_e32 v39, 0xffff0000, v4
	v_lshl_add_u64 v[4:5], v[66:67], 0, s[12:13]
	v_mov_b32_e32 v6, v146
	v_lshl_add_u64 v[4:5], v[68:69], 0, s[12:13]
	v_mov_b32_e32 v4, v147
	s_add_u32 s12, s9, s64
	s_addc_u32 s13, s10, s65
	v_mov_b32_e32 v104, v184
	s_add_u32 s12, s6, s64
	s_addc_u32 s13, s8, s65
	v_mov_b32_e32 v101, v185
	v_readlane_b32 s12, v254, 62
	v_readlane_b32 s13, v254, 63
	s_lshl_b64 s[12:13], s[12:13], 1
	v_lshlrev_b32_e32 v40, 16, v6
	v_and_b32_e32 v41, 0xffff0000, v6
	v_lshlrev_b32_e32 v34, 16, v4
	v_and_b32_e32 v35, 0xffff0000, v4
	v_lshl_add_u64 v[4:5], v[66:67], 0, s[12:13]
	v_mov_b32_e32 v6, v148
	v_lshl_add_u64 v[4:5], v[68:69], 0, s[12:13]
	v_mov_b32_e32 v4, v149
	s_add_u32 s12, s9, s66
	s_addc_u32 s13, s10, s67
	v_mov_b32_e32 v102, v186
	s_add_u32 s12, s6, s66
	s_addc_u32 s13, s8, s67
	v_mov_b32_e32 v99, v187
	s_lshl_b64 s[12:13], s[26:27], 1
	v_lshlrev_b32_e32 v36, 16, v6
	v_and_b32_e32 v37, 0xffff0000, v6
	v_lshlrev_b32_e32 v30, 16, v4
	v_and_b32_e32 v31, 0xffff0000, v4
	v_lshl_add_u64 v[4:5], v[66:67], 0, s[12:13]
	v_mov_b32_e32 v6, v150
	v_lshl_add_u64 v[4:5], v[68:69], 0, s[12:13]
	v_mov_b32_e32 v4, v151
	s_add_u32 s12, s9, s68
	s_addc_u32 s13, s10, s69
	v_mov_b32_e32 v100, v188
	s_add_u32 s12, s6, s68
; __device__ __forceinline__ void ph5_m2(const Frame& F, const Args& A) {
;     ...
;         f32x2_t uA[16], uB[16]; float nA[16], nB[16];
; #pragma unroll
;         for (int i = 0; i < 16; ++i) { const unsigned wa = *(const unsigned*)(srcA + (size_t)(16 * g + i) * 8192), wb = *(const unsigned*)(srcB + (size_t)(16 * g + i) * 8192);
;             uA[i] = (f32x2_t){bflo(wa), bfhi(wa)}; uB[i] = (f32x2_t){bflo(wb), bfhi(wb)};
;             nA[i] = snA[(16 * g + i) * 64]; nB[i] = snB[(16 * g + i) * 64]; }
;         float ApA = 1.f, ApB = 1.f, BnA = 0.f, BnB = 0.f; f32x2_t BpA = {0.f, 0.f}, BpB = {0.f, 0.f};
; #pragma unroll
;         for (int i = 0; i < 16; ++i) { const float dA = decL[hA * 128 + 16 * g + i], sA = sclL[hA * 128 + 16 * g + i], dB = decL[hB * 128 + 16 * g + i], sB = sclL[hB * 128 + 16 * g + i];
;             ApA *= dA; BpA = BpA * dA + uA[i] * sA; BnA = BnA * dA + nA[i] * sA; ApB *= dB; BpB = BpB * dB + uB[i] * sB; BnB = BnB * dB + nB[i] * sB; }
	s_addc_u32 s13, s8, s69
	v_mov_b32_e32 v97, v189
	s_lshl_b64 s[12:13], s[28:29], 1
	v_lshlrev_b32_e32 v32, 16, v6
	v_and_b32_e32 v33, 0xffff0000, v6
	v_lshlrev_b32_e32 v26, 16, v4
	v_and_b32_e32 v27, 0xffff0000, v4
	v_lshl_add_u64 v[4:5], v[66:67], 0, s[12:13]
	v_mov_b32_e32 v6, v152
	v_lshl_add_u64 v[4:5], v[68:69], 0, s[12:13]
	v_mov_b32_e32 v4, v153
	s_add_u32 s12, s9, s72
	s_addc_u32 s13, s10, s73
	v_mov_b32_e32 v98, v190
	s_add_u32 s12, s6, s72
	s_addc_u32 s13, s8, s73
	v_mov_b32_e32 v95, v191
	s_lshl_b64 s[12:13], s[30:31], 1
	v_lshlrev_b32_e32 v28, 16, v6
	v_and_b32_e32 v29, 0xffff0000, v6
	v_lshlrev_b32_e32 v22, 16, v4
	v_and_b32_e32 v23, 0xffff0000, v4
	v_lshl_add_u64 v[4:5], v[66:67], 0, s[12:13]
	v_mov_b32_e32 v6, v154
	v_lshl_add_u64 v[4:5], v[68:69], 0, s[12:13]
	v_mov_b32_e32 v4, v155
	s_add_u32 s12, s9, s76
	s_addc_u32 s13, s10, s77
	v_mov_b32_e32 v96, v192
	s_add_u32 s12, s6, s76
	s_addc_u32 s13, s8, s77
	v_mov_b32_e32 v93, v193
	s_lshl_b64 s[12:13], s[34:35], 1
	v_lshlrev_b32_e32 v24, 16, v6
	v_and_b32_e32 v25, 0xffff0000, v6
	v_lshlrev_b32_e32 v18, 16, v4
	v_and_b32_e32 v19, 0xffff0000, v4
	v_lshl_add_u64 v[4:5], v[66:67], 0, s[12:13]
	v_mov_b32_e32 v6, v156
	v_lshl_add_u64 v[4:5], v[68:69], 0, s[12:13]
	v_mov_b32_e32 v4, v157
	s_add_u32 s12, s9, s80
	s_addc_u32 s13, s10, s81
	v_mov_b32_e32 v94, v194
	s_add_u32 s12, s6, s80
	s_addc_u32 s13, s8, s81
	v_mov_b32_e32 v91, v195
	s_lshl_b64 s[12:13], s[36:37], 1
	v_lshlrev_b32_e32 v20, 16, v6
	v_and_b32_e32 v21, 0xffff0000, v6
	v_lshlrev_b32_e32 v14, 16, v4
	v_and_b32_e32 v15, 0xffff0000, v4
	v_lshl_add_u64 v[4:5], v[66:67], 0, s[12:13]
	v_mov_b32_e32 v6, v158
	v_lshl_add_u64 v[4:5], v[68:69], 0, s[12:13]
	v_mov_b32_e32 v4, v159
	s_add_u32 s12, s9, s96
	s_addc_u32 s13, s10, s97
	v_mov_b32_e32 v92, v196
	s_add_u32 s12, s6, s96
	s_addc_u32 s13, s8, s97
	v_mov_b32_e32 v89, v197
	s_lshl_b64 s[12:13], s[38:39], 1
	v_lshlrev_b32_e32 v16, 16, v6
	v_and_b32_e32 v17, 0xffff0000, v6
	v_lshlrev_b32_e32 v10, 16, v4
	v_and_b32_e32 v11, 0xffff0000, v4
	v_lshl_add_u64 v[4:5], v[66:67], 0, s[12:13]
	v_mov_b32_e32 v6, v160
	v_lshl_add_u64 v[4:5], v[68:69], 0, s[12:13]
	v_mov_b32_e32 v4, v161
	s_add_u32 s12, s9, s84
	s_addc_u32 s13, s10, s85
	v_mov_b32_e32 v90, v198
	s_add_u32 s12, s6, s84
	s_addc_u32 s13, s8, s85
	v_mov_b32_e32 v88, v199
	s_lshl_b64 s[12:13], s[40:41], 1
	v_lshlrev_b32_e32 v12, 16, v6
	v_and_b32_e32 v13, 0xffff0000, v6
	v_lshlrev_b32_e32 v6, 16, v4
	v_and_b32_e32 v7, 0xffff0000, v4
	v_lshl_add_u64 v[4:5], v[66:67], 0, s[12:13]
	v_mov_b32_e32 v9, v162
	v_lshl_add_u64 v[4:5], v[68:69], 0, s[12:13]
	s_add_u32 s12, s9, s86
	s_addc_u32 s13, s10, s87
	v_mov_b32_e32 v5, v163
	v_lshlrev_b32_e32 v8, 16, v9
	v_mov_b32_e32 v87, v200
	s_add_u32 s12, s6, s86
	s_addc_u32 s13, s8, s87
	v_mov_b32_e32 v86, v201
	s_lshl_b64 s[12:13], s[42:43], 1
	v_lshl_add_u64 v[66:67], v[66:67], 0, s[12:13]
	v_mov_b32_e32 v63, v164
	v_lshl_add_u64 v[66:67], v[68:69], 0, s[12:13]
	s_add_u32 s12, s9, s94
	s_addc_u32 s13, s10, s95
	v_mov_b32_e32 v67, v165
	s_add_u32 s10, s6, s94
	s_addc_u32 s11, s8, s95
	v_mov_b32_e32 v78, v203
	s_lshl_b32 s6, s4, 7
	s_add_i32 s6, s6, s0
	s_lshl_b32 s8, s92, 7
	s_lshl_b32 s57, s6, 2
	s_add_i32 s8, s8, s0
	s_add_i32 s18, s1, s57
	v_mov_b32_e32 v70, s18
	s_add_i32 s19, s88, s57
	s_lshl_b32 s45, s8, 2
	ds_read_b128 v[70:73], v70
	v_mov_b32_e32 v74, s19
	s_add_i32 s20, s1, s45
	ds_read_b128 v[116:119], v74
	v_mov_b32_e32 v74, s20
	s_add_i32 s21, s88, s45
	ds_read_b128 v[120:123], v74
	v_mov_b32_e32 v74, s21
	ds_read_b128 v[124:127], v74
	s_waitcnt lgkmcnt(3)
	v_mul_f32_e32 v74, 0, v70
	s_waitcnt lgkmcnt(2)
	v_pk_fma_f32 v[80:81], v[116:117], v[64:65], v[74:75] op_sel_hi:[0,1,0]
	v_pk_mul_f32 v[130:131], v[116:117], v[60:61] op_sel:[1,0]
	s_waitcnt vmcnt(16)
	v_fmac_f32_e32 v74, v82, v116
	s_waitcnt lgkmcnt(1)
	v_mul_f32_e32 v76, 0, v120
	v_pk_fma_f32 v[80:81], v[80:81], v[70:71], v[130:131] op_sel:[0,1,0]
	v_mul_f32_e32 v130, v114, v117
	s_waitcnt lgkmcnt(0)
	v_pk_fma_f32 v[128:129], v[124:125], v[58:59], v[76:77] op_sel_hi:[0,1,0]
	v_mul_f32_e32 v115, v70, v71
	v_fmac_f32_e32 v130, v74, v71
	v_pk_mul_f32 v[70:71], v[124:125], v[54:55] op_sel:[1,0]
	v_fmac_f32_e32 v76, v113, v124
	v_mul_f32_e32 v74, v120, v121
	v_pk_fma_f32 v[70:71], v[128:129], v[120:121], v[70:71] op_sel:[0,1,0]
	v_mul_f32_e32 v120, v111, v125
	v_pk_mul_f32 v[116:117], v[118:119], v[56:57] op_sel_hi:[0,1]
	v_fmac_f32_e32 v120, v76, v121
	v_mul_f32_e32 v76, v115, v72
	v_pk_fma_f32 v[80:81], v[80:81], v[72:73], v[116:117] op_sel_hi:[1,0,1]
	v_mul_f32_e32 v115, v112, v118
	v_mul_f32_e32 v118, v74, v122
	v_pk_mul_f32 v[116:117], v[126:127], v[50:51] op_sel_hi:[0,1]
	v_mov_b32_e32 v74, v119
	v_fmac_f32_e32 v115, v130, v72
	v_pk_fma_f32 v[70:71], v[70:71], v[122:123], v[116:117] op_sel_hi:[1,0,1]
	v_mov_b32_e32 v72, v73
	v_pk_mul_f32 v[116:117], v[74:75], v[52:53] op_sel_hi:[0,1]
	v_mov_b32_e32 v74, v127
	s_or_b32 s6, s57, 16
	v_pk_fma_f32 v[80:81], v[80:81], v[72:73], v[116:117] op_sel_hi:[1,0,1]
	v_mov_b32_e32 v72, v123
	v_pk_mul_f32 v[116:117], v[74:75], v[46:47] op_sel_hi:[0,1]
	v_mul_f32_e32 v121, v109, v126
	v_mul_f32_e32 v132, v110, v119
	v_pk_fma_f32 v[128:129], v[70:71], v[72:73], v[116:117] op_sel_hi:[1,0,1]
	v_fmac_f32_e32 v121, v120, v122
	v_mul_f32_e32 v76, v76, v73
	v_fmac_f32_e32 v132, v115, v73
	v_mul_f32_e32 v115, v118, v123
	v_mul_f32_e32 v74, v107, v127
	v_fmac_f32_e32 v74, v121, v123
	v_and_b32_e32 v9, 0xffff0000, v9
	s_waitcnt vmcnt(5)
	v_lshlrev_b32_e32 v4, 16, v5
	v_and_b32_e32 v5, 0xffff0000, v5
	s_andn2_b64 vcc, exec, s[16:17]
	s_waitcnt vmcnt(2)
; __device__ __forceinline__ void ph5_m2(const Frame& F, const Args& A) {
;     ...
;         for (int i = 0; i < 16; ++i) { const float dA = decL[hA * 128 + 16 * g + i], sA = sclL[hA * 128 + 16 * g + i], dB = decL[hB * 128 + 16 * g + i], sB = sclL[hB * 128 + 16 * g + i];
;             ApA *= dA; BpA = BpA * dA + uA[i] * sA; BnA = BnA * dA + nA[i] * sA; ApB *= dB; BpB = BpB * dB + uB[i] * sB; BnB = BnB * dB + nB[i] * sB; }
	v_lshlrev_b32_e32 v68, 16, v63
	v_and_b32_e32 v69, 0xffff0000, v63
	v_mov_b32_e32 v63, v202
	s_add_i32 s12, s1, s6
	s_add_i32 s13, s88, s6
	s_or_b32 s6, s45, 16
	v_mov_b32_e32 v70, s12
	v_mov_b32_e32 v116, s13
	s_add_i32 s14, s1, s6
	s_add_i32 s15, s88, s6
	ds_read_b128 v[70:73], v70
	ds_read_b128 v[116:119], v116
	v_mov_b32_e32 v120, s14
	v_mov_b32_e32 v124, s15
	ds_read_b128 v[120:123], v120
	ds_read_b128 v[124:127], v124
	s_waitcnt lgkmcnt(2)
	v_pk_mul_f32 v[130:131], v[116:117], v[48:49] op_sel_hi:[0,1]
	v_mul_f32_e32 v133, v108, v116
	v_mul_f32_e32 v76, v76, v70
	v_pk_fma_f32 v[80:81], v[80:81], v[70:71], v[130:131] op_sel_hi:[1,0,1]
	v_fmac_f32_e32 v133, v132, v70
	s_waitcnt lgkmcnt(0)
	v_pk_mul_f32 v[130:131], v[124:125], v[42:43] op_sel_hi:[0,1]
	v_mul_f32_e32 v132, v105, v124
	v_pk_fma_f32 v[128:129], v[128:129], v[120:121], v[130:131] op_sel_hi:[1,0,1]
	v_fmac_f32_e32 v132, v74, v120
	v_mul_f32_e32 v74, v76, v71
	v_pk_mul_f32 v[130:131], v[116:117], v[44:45] op_sel:[1,0]
	v_mul_f32_e32 v76, v106, v117
	v_mul_f32_e32 v115, v115, v120
	v_pk_fma_f32 v[80:81], v[80:81], v[70:71], v[130:131] op_sel:[0,1,0]
	v_fmac_f32_e32 v76, v133, v71
	v_pk_mul_f32 v[70:71], v[124:125], v[38:39] op_sel:[1,0]
	v_mul_f32_e32 v74, v74, v72
	v_pk_mul_f32 v[116:117], v[118:119], v[40:41] op_sel_hi:[0,1]
	v_mul_f32_e32 v115, v115, v121
	v_pk_fma_f32 v[70:71], v[128:129], v[120:121], v[70:71] op_sel:[0,1,0]
	v_mul_f32_e32 v120, v103, v125
	v_pk_fma_f32 v[80:81], v[80:81], v[72:73], v[116:117] op_sel_hi:[1,0,1]
	v_mul_f32_e32 v118, v104, v118
	v_pk_mul_f32 v[116:117], v[126:127], v[34:35] op_sel_hi:[0,1]
	v_mul_f32_e32 v130, v74, v73
	v_mov_b32_e32 v74, v119
	v_fmac_f32_e32 v120, v132, v121
	v_fmac_f32_e32 v118, v76, v72
	v_mul_f32_e32 v76, v115, v122
	v_pk_fma_f32 v[70:71], v[70:71], v[122:123], v[116:117] op_sel_hi:[1,0,1]
	v_mul_f32_e32 v115, v101, v126
	v_mov_b32_e32 v72, v73
	v_pk_mul_f32 v[116:117], v[74:75], v[36:37] op_sel_hi:[0,1]
	v_mov_b32_e32 v74, v127
	s_or_b32 s6, s57, 32
	v_fmac_f32_e32 v115, v120, v122
	v_pk_fma_f32 v[80:81], v[80:81], v[72:73], v[116:117] op_sel_hi:[1,0,1]
	v_mov_b32_e32 v72, v123
	v_pk_mul_f32 v[116:117], v[74:75], v[30:31] op_sel_hi:[0,1]
	v_mul_f32_e32 v74, v99, v127
	s_add_i32 s8, s1, s6
	s_add_i32 s9, s88, s6
	s_or_b32 s6, s45, 32
	v_mul_f32_e32 v132, v102, v119
	v_pk_fma_f32 v[128:129], v[70:71], v[72:73], v[116:117] op_sel_hi:[1,0,1]
	v_fmac_f32_e32 v74, v115, v123
	v_mov_b32_e32 v70, s8
	v_mov_b32_e32 v115, s9
	s_add_i32 s10, s1, s6
	v_fmac_f32_e32 v132, v118, v73
	ds_read_b128 v[70:73], v70
	ds_read_b128 v[116:119], v115
	v_mov_b32_e32 v115, s10
	s_add_i32 s11, s88, s6
	v_mul_f32_e32 v76, v76, v123
	ds_read_b128 v[120:123], v115
	v_mov_b32_e32 v115, s11
	ds_read_b128 v[124:127], v115
	s_waitcnt lgkmcnt(3)
	v_mul_f32_e32 v115, v130, v70
	s_waitcnt lgkmcnt(2)
	v_pk_mul_f32 v[130:131], v[116:117], v[32:33] op_sel_hi:[0,1]
	v_mul_f32_e32 v133, v100, v116
	v_pk_fma_f32 v[80:81], v[80:81], v[70:71], v[130:131] op_sel_hi:[1,0,1]
	v_fmac_f32_e32 v133, v132, v70
	s_waitcnt lgkmcnt(0)
; __device__ __forceinline__ void ph5_m2(const Frame& F, const Args& A) {
;     ...
;         for (int i = 0; i < 16; ++i) { const float dA = decL[hA * 128 + 16 * g + i], sA = sclL[hA * 128 + 16 * g + i], dB = decL[hB * 128 + 16 * g + i], sB = sclL[hB * 128 + 16 * g + i];
;             ApA *= dA; BpA = BpA * dA + uA[i] * sA; BnA = BnA * dA + nA[i] * sA; ApB *= dB; BpB = BpB * dB + uB[i] * sB; BnB = BnB * dB + nB[i] * sB; }
;         seg[g * 128 + 2 * l] = ApA; seg[1024 + g * 128 + 2 * l] = BpA.x; seg[1024 + g * 128 + 2 * l + 1] = BpA.y; seg[2048 + g * 64 + l] = BnA;
;         seg[3072 + g * 128 + 2 * l] = ApB; seg[3072 + 1024 + g * 128 + 2 * l] = BpB.x; seg[3072 + 1024 + g * 128 + 2 * l + 1] = BpB.y; seg[3072 + 2048 + g * 64 + l] = BnB;
;         __syncthreads();
	v_pk_mul_f32 v[130:131], v[124:125], v[26:27] op_sel_hi:[0,1]
	v_mul_f32_e32 v132, v97, v124
	v_pk_fma_f32 v[128:129], v[128:129], v[120:121], v[130:131] op_sel_hi:[1,0,1]
	v_fmac_f32_e32 v132, v74, v120
	v_mul_f32_e32 v74, v115, v71
	v_pk_mul_f32 v[130:131], v[116:117], v[28:29] op_sel:[1,0]
	v_mul_f32_e32 v115, v98, v117
	v_pk_fma_f32 v[80:81], v[80:81], v[70:71], v[130:131] op_sel:[0,1,0]
	v_fmac_f32_e32 v115, v133, v71
	v_pk_mul_f32 v[70:71], v[124:125], v[22:23] op_sel:[1,0]
	v_mul_f32_e32 v74, v74, v72
	v_pk_mul_f32 v[116:117], v[118:119], v[24:25] op_sel_hi:[0,1]
	v_mul_f32_e32 v76, v76, v120
	v_pk_fma_f32 v[70:71], v[128:129], v[120:121], v[70:71] op_sel:[0,1,0]
	v_mul_f32_e32 v120, v95, v125
	v_pk_fma_f32 v[80:81], v[80:81], v[72:73], v[116:117] op_sel_hi:[1,0,1]
	v_mul_f32_e32 v118, v96, v118
	v_pk_mul_f32 v[116:117], v[126:127], v[18:19] op_sel_hi:[0,1]
	v_mul_f32_e32 v130, v74, v73
	v_mov_b32_e32 v74, v119
	v_fmac_f32_e32 v120, v132, v121
	v_fmac_f32_e32 v118, v115, v72
	v_pk_fma_f32 v[70:71], v[70:71], v[122:123], v[116:117] op_sel_hi:[1,0,1]
	v_mul_f32_e32 v115, v93, v126
	v_mov_b32_e32 v72, v73
	v_pk_mul_f32 v[116:117], v[74:75], v[20:21] op_sel_hi:[0,1]
	v_mov_b32_e32 v74, v127
	s_or_b32 s6, s57, 48
	v_fmac_f32_e32 v115, v120, v122
	v_pk_fma_f32 v[80:81], v[80:81], v[72:73], v[116:117] op_sel_hi:[1,0,1]
	v_mov_b32_e32 v72, v123
	v_pk_mul_f32 v[116:117], v[74:75], v[14:15] op_sel_hi:[0,1]
	v_mul_f32_e32 v74, v91, v127
	s_add_i32 s46, s1, s6
	s_add_i32 s47, s88, s6
	s_or_b32 s6, s45, 48
	v_mul_f32_e32 v76, v76, v121
	v_mul_f32_e32 v132, v94, v119
	v_pk_fma_f32 v[128:129], v[70:71], v[72:73], v[116:117] op_sel_hi:[1,0,1]
	v_fmac_f32_e32 v74, v115, v123
	v_mov_b32_e32 v70, s46
	v_mov_b32_e32 v115, s47
	s_add_i32 s33, s1, s6
	v_mul_f32_e32 v76, v76, v122
	v_fmac_f32_e32 v132, v118, v73
	ds_read_b128 v[70:73], v70
	ds_read_b128 v[116:119], v115
	v_mov_b32_e32 v115, s33
	s_add_i32 s6, s88, s6
	v_mul_f32_e32 v76, v76, v123
	ds_read_b128 v[120:123], v115
	v_mov_b32_e32 v115, s6
	ds_read_b128 v[124:127], v115
	s_waitcnt lgkmcnt(3)
	v_mul_f32_e32 v115, v130, v70
	s_waitcnt lgkmcnt(2)
	v_pk_mul_f32 v[130:131], v[116:117], v[16:17] op_sel_hi:[0,1]
	v_mul_f32_e32 v133, v92, v116
	v_pk_fma_f32 v[80:81], v[80:81], v[70:71], v[130:131] op_sel_hi:[1,0,1]
	v_fmac_f32_e32 v133, v132, v70
	s_waitcnt lgkmcnt(0)
	v_pk_mul_f32 v[130:131], v[124:125], v[10:11] op_sel_hi:[0,1]
	v_mul_f32_e32 v132, v89, v124
	v_pk_fma_f32 v[128:129], v[128:129], v[120:121], v[130:131] op_sel_hi:[1,0,1]
	v_fmac_f32_e32 v132, v74, v120
	v_mul_f32_e32 v74, v115, v71
	v_pk_mul_f32 v[130:131], v[116:117], v[12:13] op_sel:[1,0]
	v_mul_f32_e32 v115, v90, v117
	v_pk_fma_f32 v[80:81], v[80:81], v[70:71], v[130:131] op_sel:[0,1,0]
	v_fmac_f32_e32 v115, v133, v71
	v_pk_mul_f32 v[70:71], v[124:125], v[6:7] op_sel:[1,0]
	v_pk_mul_f32 v[116:117], v[118:119], v[8:9] op_sel_hi:[0,1]
	v_mul_f32_e32 v76, v76, v120
	v_pk_fma_f32 v[70:71], v[128:129], v[120:121], v[70:71] op_sel:[0,1,0]
	v_mul_f32_e32 v74, v74, v72
	v_pk_fma_f32 v[80:81], v[80:81], v[72:73], v[116:117] op_sel_hi:[1,0,1]
	v_pk_mul_f32 v[116:117], v[126:127], v[4:5] op_sel_hi:[0,1]
	v_mul_f32_e32 v76, v76, v121
	v_mul_f32_e32 v118, v87, v118
	v_pk_fma_f32 v[70:71], v[70:71], v[122:123], v[116:117] op_sel_hi:[1,0,1]
	v_mul_f32_e32 v116, v74, v73
	v_mov_b32_e32 v74, v119
	s_waitcnt vmcnt(2)
	v_lshlrev_b32_e32 v66, 16, v67
	v_and_b32_e32 v67, 0xffff0000, v67
	v_mul_f32_e32 v120, v88, v125
	v_fmac_f32_e32 v118, v115, v72
	v_mul_f32_e32 v76, v76, v122
	v_mov_b32_e32 v72, v73
	v_pk_mul_f32 v[68:69], v[74:75], v[68:69] op_sel_hi:[0,1]
	s_waitcnt vmcnt(0)
	v_mul_f32_e32 v63, v63, v119
	v_mov_b32_e32 v74, v127
	v_fmac_f32_e32 v120, v132, v121
	v_mul_f32_e32 v115, v86, v126
	v_pk_fma_f32 v[68:69], v[80:81], v[72:73], v[68:69] op_sel_hi:[1,0,1]
	v_fmac_f32_e32 v63, v118, v73
	v_mul_f32_e32 v73, v76, v123
	v_mov_b32_e32 v72, v123
	v_pk_mul_f32 v[66:67], v[74:75], v[66:67] op_sel_hi:[0,1]
	v_fmac_f32_e32 v115, v120, v122
	v_pk_fma_f32 v[66:67], v[70:71], v[72:73], v[66:67] op_sel_hi:[1,0,1]
	v_mul_f32_e32 v70, v78, v127
	v_fmac_f32_e32 v70, v115, v123
	ds_write_b32 v77, v116
	ds_write_b64 v77, v[68:69] offset:4096
	ds_write_b32 v79, v63 offset:8192
	ds_write_b32 v77, v73 offset:12288
	ds_write_b64 v77, v[66:67] offset:16384
	ds_write_b32 v79, v70 offset:20480
	v_mov_b32_e32 v69, 0
	v_mov_b32_e32 v68, 0
	v_mov_b32_e32 v71, 0
	v_mov_b32_e32 v70, 0
	v_mov_b32_e32 v73, 0
	v_mov_b32_e32 v72, 0
	s_waitcnt lgkmcnt(0)
	s_barrier
	s_cbranch_vccnz .LBB0_592
	v_readlane_b32 s16, v254, 50
	v_readlane_b32 s17, v254, 51
	s_andn2_b64 vcc, exec, s[16:17]
	s_cbranch_vccnz .LBB0_588
	v_mov_b32_e32 v70, 0
	s_mov_b32 s16, 0
	v_mov_b32_e32 v63, v84
	v_mov_b32_e32 v66, v83
	v_mov_b32_e32 v71, v70
	v_mov_b32_e32 v72, v70
	v_mov_b32_e32 v73, v70
	v_mov_b32_e32 v68, v70
	v_mov_b32_e32 v69, v70
